# attention softmax row reductions by permlane16/32 swap; token tail max by DPP + permlane swaps (no ds_bpermute round trips)
# speedup vs baseline: 1.0220x; 1.0042x over previous
.Lat_A_full:
	v_max3_f32 v92, v82, v83, v84
	v_max3_f32 v93, v85, v86, v87
	v_max3_f32 v92, v92, v88, v89
	v_max_f32_e32 v92, v92, v93
	v_mov_b32_e32 v93, v92
	s_nop 1
	v_permlane16_swap_b32_e32 v92, v93
	v_max_f32_e32 v92, v92, v93
	v_mov_b32_e32 v93, v92
	s_nop 1
	v_permlane32_swap_b32_e32 v92, v93
	v_max3_f32 v180, v181, v92, v93
	v_sub_f32_e32 v94, v181, v180
	v_sub_f32_e32 v82, v82, v180
	v_sub_f32_e32 v83, v83, v180
	v_sub_f32_e32 v84, v84, v180
	v_sub_f32_e32 v85, v85, v180
	v_sub_f32_e32 v86, v86, v180
	v_sub_f32_e32 v87, v87, v180
	v_sub_f32_e32 v88, v88, v180
	v_sub_f32_e32 v89, v89, v180
	v_exp_f32_e32 v94, v94
	v_exp_f32_e32 v82, v82
	v_exp_f32_e32 v83, v83
	v_exp_f32_e32 v84, v84
	v_exp_f32_e32 v85, v85
	v_exp_f32_e32 v86, v86
	v_exp_f32_e32 v87, v87
	v_exp_f32_e32 v88, v88
	v_exp_f32_e32 v89, v89
	v_add_f32_e32 v92, v82, v83
	v_add_f32_e32 v93, v84, v85
	v_add_f32_e32 v97, v86, v87
	v_add_f32_e32 v92, v92, v93
	v_add_f32_e32 v96, v88, v89
	v_add_f32_e32 v97, v97, v96
	v_add_f32_e32 v92, v92, v97
	v_mov_b32_e32 v93, v92
	v_mov_b32_e32 v181, v180
	v_cvt_pk_bf16_f32 v82, v82, v83
	v_cvt_pk_bf16_f32 v83, v84, v85
	v_permlane16_swap_b32_e32 v92, v93
	v_add_f32_e32 v92, v92, v93
	v_mov_b32_e32 v93, v92
	v_cvt_pk_bf16_f32 v84, v86, v87
	v_cvt_pk_bf16_f32 v85, v88, v89
	v_permlane32_swap_b32_e32 v92, v93
	v_add_f32_e32 v92, v92, v93
	v_fma_f32 v179, v179, v94, v92
	v_pk_mul_f32 v[2:3], v[2:3], v[94:95] op_sel_hi:[1,0]
	v_pk_mul_f32 v[4:5], v[4:5], v[94:95] op_sel_hi:[1,0]
	v_pk_mul_f32 v[6:7], v[6:7], v[94:95] op_sel_hi:[1,0]
	v_pk_mul_f32 v[8:9], v[8:9], v[94:95] op_sel_hi:[1,0]
	v_pk_mul_f32 v[10:11], v[10:11], v[94:95] op_sel_hi:[1,0]
	v_pk_mul_f32 v[12:13], v[12:13], v[94:95] op_sel_hi:[1,0]
	v_pk_mul_f32 v[14:15], v[14:15], v[94:95] op_sel_hi:[1,0]
	v_pk_mul_f32 v[16:17], v[16:17], v[94:95] op_sel_hi:[1,0]
	v_pk_mul_f32 v[18:19], v[18:19], v[94:95] op_sel_hi:[1,0]
	v_pk_mul_f32 v[20:21], v[20:21], v[94:95] op_sel_hi:[1,0]
	v_pk_mul_f32 v[22:23], v[22:23], v[94:95] op_sel_hi:[1,0]
	v_pk_mul_f32 v[24:25], v[24:25], v[94:95] op_sel_hi:[1,0]
	v_pk_mul_f32 v[26:27], v[26:27], v[94:95] op_sel_hi:[1,0]
	v_pk_mul_f32 v[28:29], v[28:29], v[94:95] op_sel_hi:[1,0]
	v_pk_mul_f32 v[30:31], v[30:31], v[94:95] op_sel_hi:[1,0]
	v_pk_mul_f32 v[32:33], v[32:33], v[94:95] op_sel_hi:[1,0]
	ds_read_b64_tr_b16 v[86:87], v231
	ds_read_b64_tr_b16 v[88:89], v231 offset:4096
	ds_read_b64_tr_b16 v[244:245], v232
	ds_read_b64_tr_b16 v[246:247], v232 offset:4096
	s_waitcnt lgkmcnt(2)
	v_mfma_f32_16x16x32_bf16 v[2:5], v[86:89], v[82:85], v[2:5]
	ds_read_b64_tr_b16 v[86:87], v233
	ds_read_b64_tr_b16 v[88:89], v233 offset:4096
	s_waitcnt lgkmcnt(2)
	v_mfma_f32_16x16x32_bf16 v[6:9], v[244:247], v[82:85], v[6:9]
	ds_read_b64_tr_b16 v[244:245], v234
	ds_read_b64_tr_b16 v[246:247], v234 offset:4096
	s_waitcnt lgkmcnt(2)
	v_mfma_f32_16x16x32_bf16 v[10:13], v[86:89], v[82:85], v[10:13]
	ds_read_b64_tr_b16 v[86:87], v235
	ds_read_b64_tr_b16 v[88:89], v235 offset:4096
	s_waitcnt lgkmcnt(2)
	v_mfma_f32_16x16x32_bf16 v[14:17], v[244:247], v[82:85], v[14:17]
	ds_read_b64_tr_b16 v[244:245], v236
	ds_read_b64_tr_b16 v[246:247], v236 offset:4096
	s_waitcnt lgkmcnt(2)
	v_mfma_f32_16x16x32_bf16 v[18:21], v[86:89], v[82:85], v[18:21]
	ds_read_b64_tr_b16 v[86:87], v237
	ds_read_b64_tr_b16 v[88:89], v237 offset:4096
	s_waitcnt lgkmcnt(2)
	v_mfma_f32_16x16x32_bf16 v[22:25], v[244:247], v[82:85], v[22:25]
	ds_read_b64_tr_b16 v[244:245], v238
	ds_read_b64_tr_b16 v[246:247], v238 offset:4096
	s_waitcnt lgkmcnt(2)
	v_mfma_f32_16x16x32_bf16 v[30:33], v[86:89], v[82:85], v[30:33]
	s_waitcnt lgkmcnt(0)
	v_mfma_f32_16x16x32_bf16 v[26:29], v[244:247], v[82:85], v[26:29]
	s_add_u32 s11, s11, 1
	s_add_u32 s22, s22, 32
	v_add_u32_e32 v239, 0x80, v239
	s_cmp_lt_u32 s11, s10
	s_cbranch_scc0 .Lat_done

.Lat_B_full:
	v_max3_f32 v92, v82, v83, v84
	v_max3_f32 v93, v85, v86, v87
	v_max3_f32 v92, v92, v88, v89
	v_max_f32_e32 v92, v92, v93
	v_mov_b32_e32 v93, v92
	s_nop 1
	v_permlane16_swap_b32_e32 v92, v93
	v_max_f32_e32 v92, v92, v93
	v_mov_b32_e32 v93, v92
	s_nop 1
	v_permlane32_swap_b32_e32 v92, v93
	v_max3_f32 v180, v181, v92, v93
	v_sub_f32_e32 v94, v181, v180
	v_sub_f32_e32 v82, v82, v180
	v_sub_f32_e32 v83, v83, v180
	v_sub_f32_e32 v84, v84, v180
	v_sub_f32_e32 v85, v85, v180
	v_sub_f32_e32 v86, v86, v180
	v_sub_f32_e32 v87, v87, v180
	v_sub_f32_e32 v88, v88, v180
	v_sub_f32_e32 v89, v89, v180
	v_exp_f32_e32 v94, v94
	v_exp_f32_e32 v82, v82
	v_exp_f32_e32 v83, v83
	v_exp_f32_e32 v84, v84
	v_exp_f32_e32 v85, v85
	v_exp_f32_e32 v86, v86
	v_exp_f32_e32 v87, v87
	v_exp_f32_e32 v88, v88
	v_exp_f32_e32 v89, v89
	v_add_f32_e32 v92, v82, v83
	v_add_f32_e32 v93, v84, v85
	v_add_f32_e32 v97, v86, v87
	v_add_f32_e32 v92, v92, v93
	v_add_f32_e32 v96, v88, v89
	v_add_f32_e32 v97, v97, v96
	v_add_f32_e32 v92, v92, v97
	v_mov_b32_e32 v93, v92
	v_mov_b32_e32 v181, v180
	v_cvt_pk_bf16_f32 v82, v82, v83
	v_cvt_pk_bf16_f32 v83, v84, v85
	v_permlane16_swap_b32_e32 v92, v93
	v_add_f32_e32 v92, v92, v93
	v_mov_b32_e32 v93, v92
	v_cvt_pk_bf16_f32 v84, v86, v87
	v_cvt_pk_bf16_f32 v85, v88, v89
	v_permlane32_swap_b32_e32 v92, v93
	v_add_f32_e32 v92, v92, v93
	v_fma_f32 v179, v179, v94, v92
	v_pk_mul_f32 v[2:3], v[2:3], v[94:95] op_sel_hi:[1,0]
	v_pk_mul_f32 v[4:5], v[4:5], v[94:95] op_sel_hi:[1,0]
	v_pk_mul_f32 v[6:7], v[6:7], v[94:95] op_sel_hi:[1,0]
	v_pk_mul_f32 v[8:9], v[8:9], v[94:95] op_sel_hi:[1,0]
	v_pk_mul_f32 v[10:11], v[10:11], v[94:95] op_sel_hi:[1,0]
	v_pk_mul_f32 v[12:13], v[12:13], v[94:95] op_sel_hi:[1,0]
	v_pk_mul_f32 v[14:15], v[14:15], v[94:95] op_sel_hi:[1,0]
	v_pk_mul_f32 v[16:17], v[16:17], v[94:95] op_sel_hi:[1,0]
	v_pk_mul_f32 v[18:19], v[18:19], v[94:95] op_sel_hi:[1,0]
	v_pk_mul_f32 v[20:21], v[20:21], v[94:95] op_sel_hi:[1,0]
	v_pk_mul_f32 v[22:23], v[22:23], v[94:95] op_sel_hi:[1,0]
	v_pk_mul_f32 v[24:25], v[24:25], v[94:95] op_sel_hi:[1,0]
	v_pk_mul_f32 v[26:27], v[26:27], v[94:95] op_sel_hi:[1,0]
	v_pk_mul_f32 v[28:29], v[28:29], v[94:95] op_sel_hi:[1,0]
	v_pk_mul_f32 v[30:31], v[30:31], v[94:95] op_sel_hi:[1,0]
	v_pk_mul_f32 v[32:33], v[32:33], v[94:95] op_sel_hi:[1,0]
	ds_read_b64_tr_b16 v[86:87], v231
	ds_read_b64_tr_b16 v[88:89], v231 offset:4096
	ds_read_b64_tr_b16 v[244:245], v232
	ds_read_b64_tr_b16 v[246:247], v232 offset:4096
	s_waitcnt lgkmcnt(2)
	v_mfma_f32_16x16x32_bf16 v[2:5], v[86:89], v[82:85], v[2:5]
	ds_read_b64_tr_b16 v[86:87], v233
	ds_read_b64_tr_b16 v[88:89], v233 offset:4096
	s_waitcnt lgkmcnt(2)
	v_mfma_f32_16x16x32_bf16 v[6:9], v[244:247], v[82:85], v[6:9]
	ds_read_b64_tr_b16 v[244:245], v234
	ds_read_b64_tr_b16 v[246:247], v234 offset:4096
	s_waitcnt lgkmcnt(2)
	v_mfma_f32_16x16x32_bf16 v[10:13], v[86:89], v[82:85], v[10:13]
	ds_read_b64_tr_b16 v[86:87], v235
	ds_read_b64_tr_b16 v[88:89], v235 offset:4096
	s_waitcnt lgkmcnt(2)
	v_mfma_f32_16x16x32_bf16 v[14:17], v[244:247], v[82:85], v[14:17]
	ds_read_b64_tr_b16 v[244:245], v236
	ds_read_b64_tr_b16 v[246:247], v236 offset:4096
	s_waitcnt lgkmcnt(2)
	v_mfma_f32_16x16x32_bf16 v[18:21], v[86:89], v[82:85], v[18:21]
	ds_read_b64_tr_b16 v[86:87], v237
	ds_read_b64_tr_b16 v[88:89], v237 offset:4096
	s_waitcnt lgkmcnt(2)
	v_mfma_f32_16x16x32_bf16 v[22:25], v[244:247], v[82:85], v[22:25]
	ds_read_b64_tr_b16 v[244:245], v238
	ds_read_b64_tr_b16 v[246:247], v238 offset:4096
	s_waitcnt lgkmcnt(2)
	v_mfma_f32_16x16x32_bf16 v[30:33], v[86:89], v[82:85], v[30:33]
	s_waitcnt lgkmcnt(0)
	v_mfma_f32_16x16x32_bf16 v[26:29], v[244:247], v[82:85], v[26:29]
	s_add_u32 s11, s11, 1
	s_add_u32 s22, s22, 32
	v_add_u32_e32 v239, 0x80, v239
	s_cmp_lt_u32 s11, s10
	s_cbranch_scc1 .Lat_A

.Lcv_b_noi:
	v_ashrrev_i32_e32 v34, 2, v151
	s_lshl_b64 s[0:1], s[96:97], 6
	v_ashrrev_i32_e32 v35, 31, v34
	s_add_u32 s0, s72, s0
	s_addc_u32 s1, s73, s1
	v_lshlrev_b64 v[36:37], 2, v[34:35]
	v_lshl_add_u64 v[38:39], s[0:1], 0, v[36:37]
	s_add_u32 s0, s96, 0x2000
	s_addc_u32 s1, s97, 0
	s_lshl_b64 s[2:3], s[0:1], 6
	s_add_u32 s2, s72, s2
	s_addc_u32 s3, s73, s3
	s_add_u32 s4, s96, 0x4000
	s_addc_u32 s5, s97, 0
	v_lshl_add_u64 v[40:41], s[2:3], 0, v[36:37]
	s_lshl_b64 s[2:3], s[4:5], 6
	s_add_u32 s2, s72, s2
	s_addc_u32 s3, s73, s3
	v_lshl_add_u64 v[36:37], s[2:3], 0, v[36:37]
	global_load_dword v43, v[38:39], off
	global_load_dword v69, v[40:41], off
	global_load_dword v70, v[36:37], off
	v_div_scale_f32 v46, s[2:3], v179, v179, 1.0
	v_rcp_f32_e32 v47, v46
	s_lshl_b64 s[2:3], s[96:97], 12
	s_add_u32 s6, s86, s2
	v_lshlrev_b32_e32 v44, 7, v34
	v_fma_f32 v35, -v46, v47, 1.0
	v_fmac_f32_e32 v47, v35, v47
	v_lshlrev_b32_e32 v35, 5, v151
	s_addc_u32 s7, s87, s3
	v_ashrrev_i32_e32 v45, 31, v44
	s_lshl_b64 s[0:1], s[0:1], 12
	v_and_b32_e32 v42, 0x60, v35
	v_lshlrev_b64 v[34:35], 1, v[44:45]
	s_add_u32 s0, s86, s0
	v_lshl_add_u64 v[36:37], s[6:7], 0, v[34:35]
	v_lshlrev_b32_e32 v146, 1, v42
	s_addc_u32 s1, s87, s1
	v_div_scale_f32 v48, vcc, 1.0, v179, 1.0
	s_waitcnt vmcnt(5)
	v_lshl_add_u64 v[62:63], v[36:37], 0, v[146:147]
	v_lshl_add_u64 v[36:37], s[0:1], 0, v[34:35]
	s_lshl_b64 s[0:1], s[4:5], 12
	v_mul_f32_e32 v49, v48, v47
	s_add_u32 s0, s86, s0
	s_waitcnt vmcnt(4)
	v_fma_f32 v50, -v46, v49, v48
	s_addc_u32 s1, s87, s1
	v_fmac_f32_e32 v49, v50, v47
	v_lshl_add_u64 v[34:35], s[0:1], 0, v[34:35]
	v_fma_f32 v46, -v46, v49, v48
	v_lshl_add_u64 v[64:65], v[36:37], 0, v[146:147]
	v_lshl_add_u64 v[66:67], v[34:35], 0, v[146:147]
	global_load_dwordx4 v[74:77], v[62:63], off
	global_load_dwordx4 v[34:37], v[62:63], off offset:48
	global_load_dwordx4 v[78:81], v[64:65], off
	global_load_dwordx4 v[38:41], v[64:65], off offset:48
	global_load_dwordx4 v[82:85], v[66:67], off
	v_div_fmas_f32 v46, v46, v47, v49
	v_div_fixup_f32 v68, v46, v179, 1.0
	global_load_dwordx4 v[86:89], v[62:63], off offset:32
	global_load_dwordx4 v[90:93], v[62:63], off offset:16
	global_load_dwordx4 v[94:97], v[64:65], off offset:32
	global_load_dwordx4 v[98:101], v[64:65], off offset:16
	global_load_dwordx4 v[102:105], v[66:67], off offset:32
	global_load_dwordx4 v[106:109], v[66:67], off offset:16
	s_waitcnt vmcnt(12)
	v_pk_mul_f32 v[58:59], v[4:5], v[68:69] op_sel_hi:[1,0]
	v_pk_mul_f32 v[54:55], v[8:9], v[68:69] op_sel_hi:[1,0]
	v_pk_mul_f32 v[60:61], v[2:3], v[68:69] op_sel_hi:[1,0]
	v_max_f32_e64 v2, |v58|, |v59|
	v_pk_mul_f32 v[56:57], v[6:7], v[68:69] op_sel_hi:[1,0]
	v_max_f32_e64 v3, |v54|, |v55|
	v_max3_f32 v2, |v60|, |v61|, v2
	v_max3_f32 v3, |v56|, |v57|, v3
	v_pk_mul_f32 v[50:51], v[12:13], v[68:69] op_sel_hi:[1,0]
	v_pk_mul_f32 v[46:47], v[16:17], v[68:69] op_sel_hi:[1,0]
	v_max3_f32 v2, v2, 0, v3
	v_pk_mul_f32 v[52:53], v[10:11], v[68:69] op_sel_hi:[1,0]
	v_max_f32_e64 v3, |v50|, |v51|
	v_pk_mul_f32 v[48:49], v[14:15], v[68:69] op_sel_hi:[1,0]
	v_max_f32_e64 v4, |v46|, |v47|
	v_max3_f32 v3, |v52|, |v53|, v3
	v_max3_f32 v4, |v48|, |v49|, v4
	v_pk_mul_f32 v[20:21], v[20:21], v[68:69] op_sel_hi:[1,0]
	v_pk_mul_f32 v[14:15], v[24:25], v[68:69] op_sel_hi:[1,0]
	v_max3_f32 v2, v2, v3, v4
	v_pk_mul_f32 v[18:19], v[18:19], v[68:69] op_sel_hi:[1,0]
	v_max_f32_e64 v3, |v20|, |v21|
	v_pk_mul_f32 v[16:17], v[22:23], v[68:69] op_sel_hi:[1,0]
	v_max_f32_e64 v4, |v14|, |v15|
	v_max3_f32 v3, |v18|, |v19|, v3
	v_max3_f32 v4, |v16|, |v17|, v4
	v_max3_f32 v2, v2, v3, v4
	s_waitcnt vmcnt(11)
	v_max3_f32 v4, v43, v69, v70
	v_sub_f32_e32 v5, v43, v4
	v_exp_f32_e32 v110, v5
	v_sub_f32_e32 v5, v69, v4
	v_exp_f32_e32 v5, v5
	v_sub_f32_e32 v4, v70, v4
	v_exp_f32_e32 v111, v4
	v_pk_mul_f32 v[10:11], v[32:33], v[68:69] op_sel_hi:[1,0]
	v_add_f32_e32 v4, v110, v5
	v_pk_mul_f32 v[6:7], v[28:29], v[68:69] op_sel_hi:[1,0]
	v_add_f32_e32 v4, v111, v4
	v_div_scale_f32 v22, s[0:1], v4, v4, 1.0
	v_rcp_f32_e32 v23, v22
	v_pk_mul_f32 v[12:13], v[30:31], v[68:69] op_sel_hi:[1,0]
	v_max_f32_e64 v3, |v10|, |v11|
	v_pk_mul_f32 v[8:9], v[26:27], v[68:69] op_sel_hi:[1,0]
	v_max_f32_e64 v24, |v6|, |v7|
	v_max3_f32 v3, |v12|, |v13|, v3
	v_max3_f32 v24, |v8|, |v9|, v24
	v_max3_f32 v43, v2, v3, v24
	v_fma_f32 v2, -v22, v23, 1.0
	v_fmac_f32_e32 v23, v2, v23
	v_div_scale_f32 v2, vcc, 1.0, v4, 1.0
	v_mul_f32_e32 v3, v2, v23
	v_fma_f32 v24, -v22, v3, v2
	v_fmac_f32_e32 v3, v24, v23
	v_fma_f32 v2, -v22, v3, v2
	v_div_fmas_f32 v2, v2, v23, v3
	v_div_fixup_f32 v112, v2, v4, 1.0
	v_mul_f32_e32 v113, v5, v112
	global_load_dwordx4 v[2:5], v[66:67], off offset:48
	s_waitcnt vmcnt(9)
	v_lshlrev_b32_e32 v22, 16, v78
	v_mul_f32_e32 v62, v113, v22
	v_and_b32_e32 v22, 0xffff0000, v78
	v_mul_f32_e32 v67, v113, v22
	v_lshlrev_b32_e32 v22, 16, v79
	v_mul_f32_e32 v71, v113, v22
	v_and_b32_e32 v22, 0xffff0000, v79
	s_waitcnt vmcnt(7)
	v_lshlrev_b32_e32 v115, 16, v82
	v_and_b32_e32 v78, 0xffff0000, v82
	v_lshlrev_b32_e32 v82, 16, v75
	v_and_b32_e32 v118, 0xffff0000, v75
	v_mul_f32_e32 v75, v113, v22
	v_lshlrev_b32_e32 v22, 16, v80
	v_mul_f32_e32 v32, v113, v22
	v_and_b32_e32 v22, 0xffff0000, v80
	v_mul_f32_e32 v66, v113, v22
	v_lshlrev_b32_e32 v22, 16, v81
	v_mul_f32_e32 v70, v113, v22
	v_and_b32_e32 v22, 0xffff0000, v81
	v_lshlrev_b32_e32 v114, 16, v74
	v_and_b32_e32 v116, 0xffff0000, v74
	v_mul_f32_e32 v74, v113, v22
	s_waitcnt vmcnt(3)
	v_lshlrev_b32_e32 v22, 16, v98
	v_mul_f32_e32 v31, v113, v22
	v_and_b32_e32 v22, 0xffff0000, v98
	v_mul_f32_e32 v65, v113, v22
	v_lshlrev_b32_e32 v22, 16, v99
	v_mul_f32_e32 v69, v113, v22
	v_and_b32_e32 v22, 0xffff0000, v99
	v_mul_f32_e32 v73, v113, v22
	v_lshlrev_b32_e32 v22, 16, v100
	v_mul_f32_e32 v29, v113, v22
	v_and_b32_e32 v22, 0xffff0000, v100
	v_mul_f32_e32 v63, v113, v22
	v_lshlrev_b32_e32 v22, 16, v101
	v_mul_f32_e32 v68, v113, v22
	v_and_b32_e32 v22, 0xffff0000, v101
	v_mul_f32_e32 v72, v113, v22
	v_lshlrev_b32_e32 v22, 16, v94
	v_mul_f32_e32 v24, v113, v22
	v_and_b32_e32 v22, 0xffff0000, v94
	v_mul_f32_e32 v27, v113, v22
	v_lshlrev_b32_e32 v22, 16, v95
	v_mul_f32_e32 v30, v113, v22
	v_and_b32_e32 v22, 0xffff0000, v95
	v_mul_f32_e32 v64, v113, v22
	v_lshlrev_b32_e32 v22, 16, v96
	v_mul_f32_e32 v23, v113, v22
	v_and_b32_e32 v22, 0xffff0000, v96
	v_mul_f32_e32 v26, v113, v22
	v_lshlrev_b32_e32 v22, 16, v97
	v_mul_f32_e32 v28, v113, v22
	v_and_b32_e32 v22, 0xffff0000, v97
	v_mul_f32_e32 v33, v113, v22
	v_lshlrev_b32_e32 v22, 16, v38
	v_and_b32_e32 v25, 0xffff0000, v38
	v_lshlrev_b32_e32 v130, 16, v39
	v_and_b32_e32 v131, 0xffff0000, v39
	v_pk_mul_f32 v[38:39], v[110:111], v[112:113] op_sel_hi:[1,0]
	v_lshlrev_b32_e32 v117, 16, v83
	v_and_b32_e32 v79, 0xffff0000, v83
	v_lshlrev_b32_e32 v83, 16, v76
	v_lshlrev_b32_e32 v119, 16, v84
	v_and_b32_e32 v76, 0xffff0000, v76
	v_and_b32_e32 v80, 0xffff0000, v84
	v_lshlrev_b32_e32 v84, 16, v77
	v_and_b32_e32 v77, 0xffff0000, v77
	v_fmac_f32_e32 v62, v38, v114
	v_fmac_f32_e32 v67, v38, v116
	v_fmac_f32_e32 v71, v38, v82
	v_fmac_f32_e32 v75, v38, v118
	v_lshlrev_b32_e32 v120, 16, v85
	v_and_b32_e32 v81, 0xffff0000, v85
	v_lshlrev_b32_e32 v85, 16, v90
	s_waitcnt vmcnt(1)
	v_lshlrev_b32_e32 v121, 16, v106
	v_and_b32_e32 v90, 0xffff0000, v90
	v_and_b32_e32 v98, 0xffff0000, v106
	v_lshlrev_b32_e32 v106, 16, v91
	v_and_b32_e32 v91, 0xffff0000, v91
	v_fmac_f32_e32 v62, v39, v115
	v_fmac_f32_e32 v67, v39, v78
	v_fmac_f32_e32 v71, v39, v117
	v_fmac_f32_e32 v75, v39, v79
	v_fmac_f32_e32 v32, v38, v83
	v_fmac_f32_e32 v66, v38, v76
	v_fmac_f32_e32 v70, v38, v84
	v_fmac_f32_e32 v74, v38, v77
	v_lshlrev_b32_e32 v122, 16, v107
	v_and_b32_e32 v99, 0xffff0000, v107
	v_lshlrev_b32_e32 v107, 16, v92
	v_lshlrev_b32_e32 v123, 16, v108
	v_and_b32_e32 v92, 0xffff0000, v92
	v_and_b32_e32 v100, 0xffff0000, v108
	v_lshlrev_b32_e32 v108, 16, v93
	v_and_b32_e32 v93, 0xffff0000, v93
	v_max_f32_e64 v78, |v62|, |v67|
	v_max_f32_e64 v79, |v71|, |v75|
	v_fmac_f32_e32 v32, v39, v119
	v_fmac_f32_e32 v66, v39, v80
	v_fmac_f32_e32 v70, v39, v120
	v_fmac_f32_e32 v74, v39, v81
	v_fmac_f32_e32 v31, v38, v85
	v_fmac_f32_e32 v65, v38, v90
	v_fmac_f32_e32 v69, v38, v106
	v_fmac_f32_e32 v73, v38, v91
	v_lshlrev_b32_e32 v124, 16, v109
	v_and_b32_e32 v101, 0xffff0000, v109
	v_lshlrev_b32_e32 v109, 16, v86
	v_lshlrev_b32_e32 v125, 16, v102
	v_and_b32_e32 v86, 0xffff0000, v86
	v_and_b32_e32 v94, 0xffff0000, v102
	v_lshlrev_b32_e32 v102, 16, v87
	v_and_b32_e32 v87, 0xffff0000, v87
	v_max3_f32 v43, v43, v78, v79
	v_max_f32_e64 v76, |v32|, |v66|
	v_max_f32_e64 v77, |v70|, |v74|
	v_fmac_f32_e32 v31, v39, v121
	v_fmac_f32_e32 v65, v39, v98
	v_fmac_f32_e32 v69, v39, v122
	v_fmac_f32_e32 v73, v39, v99
	v_fmac_f32_e32 v29, v38, v107
	v_fmac_f32_e32 v63, v38, v92
	v_fmac_f32_e32 v68, v38, v108
	v_fmac_f32_e32 v72, v38, v93
	v_lshlrev_b32_e32 v126, 16, v103
	v_and_b32_e32 v95, 0xffff0000, v103
	v_lshlrev_b32_e32 v103, 16, v88
	v_lshlrev_b32_e32 v127, 16, v104
	v_and_b32_e32 v88, 0xffff0000, v88
	v_and_b32_e32 v96, 0xffff0000, v104
	v_lshlrev_b32_e32 v104, 16, v89
	v_and_b32_e32 v89, 0xffff0000, v89
	v_max3_f32 v43, v43, v76, v77
	v_max_f32_e64 v76, |v31|, |v65|
	v_max_f32_e64 v77, |v69|, |v73|
	v_fmac_f32_e32 v29, v39, v123
	v_fmac_f32_e32 v63, v39, v100
	v_fmac_f32_e32 v68, v39, v124
	v_fmac_f32_e32 v72, v39, v101
	v_fmac_f32_e32 v24, v38, v109
	v_fmac_f32_e32 v27, v38, v86
	v_fmac_f32_e32 v30, v38, v102
	v_fmac_f32_e32 v64, v38, v87
	v_lshlrev_b32_e32 v128, 16, v105
	v_and_b32_e32 v97, 0xffff0000, v105
	v_max3_f32 v43, v43, v76, v77
	v_max_f32_e64 v76, |v29|, |v63|
	v_max_f32_e64 v77, |v68|, |v72|
	v_fmac_f32_e32 v24, v39, v125
	v_fmac_f32_e32 v27, v39, v94
	v_fmac_f32_e32 v30, v39, v126
	v_fmac_f32_e32 v64, v39, v95
	v_fmac_f32_e32 v23, v38, v103
	v_fmac_f32_e32 v26, v38, v88
	v_fmac_f32_e32 v28, v38, v104
	v_fmac_f32_e32 v33, v38, v89
	v_max3_f32 v43, v43, v76, v77
	v_max_f32_e64 v76, |v24|, |v27|
	v_max_f32_e64 v77, |v30|, |v64|
	v_fmac_f32_e32 v23, v39, v127
	v_fmac_f32_e32 v26, v39, v96
	v_fmac_f32_e32 v28, v39, v128
	v_fmac_f32_e32 v33, v39, v97
	v_max3_f32 v43, v43, v76, v77
	v_max_f32_e64 v76, |v23|, |v26|
	v_max_f32_e64 v77, |v28|, |v33|
	v_lshlrev_b32_e32 v105, 16, v34
	v_and_b32_e32 v34, 0xffff0000, v34
	v_mul_f32_e32 v25, v113, v25
	v_max3_f32 v43, v43, v76, v77
	s_waitcnt vmcnt(0)
	v_lshlrev_b32_e32 v77, 16, v3
	v_lshlrev_b32_e32 v76, 16, v35
	v_lshlrev_b32_e32 v129, 16, v2
	v_and_b32_e32 v2, 0xffff0000, v2
	v_fmac_f32_e32 v25, v38, v34
	v_pk_mul_f32 v[76:77], v[38:39], v[76:77]
	v_fmac_f32_e32 v25, v39, v2
	v_fma_f32 v2, v113, v130, v76
	v_add_f32_e32 v2, v2, v77
	v_and_b32_e32 v77, 0xffff0000, v3
	v_and_b32_e32 v76, 0xffff0000, v35
	v_mul_f32_e32 v22, v113, v22
	v_pk_mul_f32 v[34:35], v[38:39], v[76:77]
	v_fmac_f32_e32 v22, v38, v105
	v_fma_f32 v3, v113, v131, v34
	v_fmac_f32_e32 v22, v39, v129
	v_add_f32_e32 v34, v3, v35
	v_lshlrev_b32_e32 v77, 16, v4
	v_lshlrev_b32_e32 v76, 16, v36
	v_lshlrev_b32_e32 v132, 16, v40
	v_max_f32_e64 v78, |v22|, |v25|
	v_max_f32_e64 v3, |v2|, |v34|
	v_pk_mul_f32 v[76:77], v[38:39], v[76:77]
	v_max3_f32 v43, v43, v78, v3
	v_fma_f32 v3, v113, v132, v76
	v_add_f32_e32 v3, v3, v77
	v_and_b32_e32 v77, 0xffff0000, v4
	v_and_b32_e32 v76, 0xffff0000, v36
	v_and_b32_e32 v40, 0xffff0000, v40
	v_pk_mul_f32 v[76:77], v[38:39], v[76:77]
	v_lshlrev_b32_e32 v133, 16, v41
	v_fma_f32 v4, v113, v40, v76
	v_add_f32_e32 v4, v4, v77
	v_lshlrev_b32_e32 v77, 16, v5
	v_lshlrev_b32_e32 v76, 16, v37
	v_pk_mul_f32 v[76:77], v[38:39], v[76:77]
	v_and_b32_e32 v40, 0xffff0000, v37
	v_fma_f32 v35, v113, v133, v76
	v_and_b32_e32 v76, 0xffff0000, v41
	v_and_b32_e32 v41, 0xffff0000, v5
	v_pk_mul_f32 v[36:37], v[38:39], v[40:41]
	v_add_f32_e32 v35, v35, v77
	v_fma_f32 v5, v113, v76, v36
	v_add_f32_e32 v5, v5, v37
	v_max_f32_e64 v78, |v3|, |v4|
	v_max_f32_e64 v36, |v35|, |v5|
	v_max3_f32 v36, v43, v78, v36
	v_cmp_eq_u32_e32 vcc, 0, v151
	s_nop 0
	v_max_f32_dpp v36, v36, v36 quad_perm:[1,0,3,2] row_mask:0xf bank_mask:0xf
	s_nop 1
	v_max_f32_dpp v36, v36, v36 quad_perm:[2,3,0,1] row_mask:0xf bank_mask:0xf
	s_nop 1
	v_max_f32_dpp v36, v36, v36 row_half_mirror row_mask:0xf bank_mask:0xf
	s_nop 1
	v_max_f32_dpp v36, v36, v36 row_mirror row_mask:0xf bank_mask:0xf
	s_nop 1
	v_mov_b32_e32 v37, v36
	s_nop 1
	v_permlane16_swap_b32_e32 v36, v37
	v_max_f32_e32 v36, v36, v37
	v_mov_b32_e32 v37, v36
	s_nop 1
	v_permlane32_swap_b32_e32 v36, v37
	v_max_f32_e32 v36, v36, v37
	v_cmp_lt_f32_e64 s[0:1], 0, v36
	s_and_saveexec_b64 s[4:5], vcc
	s_cbranch_execz .LBB0_1129
	s_lshl_b64 s[6:7], s[96:97], 2
	v_readlane_b32 s8, v242, 39
	v_readlane_b32 s9, v242, 40
	s_add_u32 s6, s8, s6
	v_mul_f32_e32 v37, 0x3c010204, v36
	s_addc_u32 s7, s9, s7
	v_cndmask_b32_e64 v37, 1.0, v37, s[0:1]
	global_store_dword v147, v37, s[6:7]
